# speedup vs baseline: 1.0118x; 1.0118x over previous
_Z9ssim_mainPKfS0_S0_Pf:
	v_readfirstlane_b32 s29, v0
	s_load_dwordx4 s[4:7], s[0:1], 0x0
	s_load_dwordx4 s[8:11], s[0:1], 0x10
	s_mov_b32 s51, 0x44800000
	s_mov_b32 s38, 0
	s_mov_b32 s39, -1
	s_lshr_b32 s12, s29, 6
	s_and_b32 s13, s2, 7
	s_lshl_b32 s13, s13, 5
	s_lshr_b32 s14, s2, 3
	s_add_u32 s13, s13, s14
	s_lshr_b32 s14, s13, 3
	s_and_b32 s15, s13, 7
	s_lshl_b32 s16, s14, 20
	s_lshl_b32 s17, s15, 17
	s_add_u32 s16, s16, s17
	s_lshl_b32 s17, s12, 8
	s_add_u32 s16, s16, s17
	s_lshl_b32 s27, s12, 2
	s_add_u32 s27, s27, 0x10000
	v_and_b32_e32 v8, 63, v0
	v_and_b32_e32 v169, 15, v0
	v_bfe_u32 v164, v0, 4, 2
	v_lshrrev_b32_e32 v167, 2, v169
	v_lshlrev_b32_e32 v167, 5, v167
	v_and_b32_e32 v168, 1, v169
	v_lshl_or_b32 v167, v168, 4, v167
	v_bfe_u32 v168, v169, 1, 1
	v_lshl_or_b32 v167, v168, 7, v167
	v_lshl_or_b32 v9, v164, 14, v167
	v_and_b32_e32 v168, 1, v164
	v_lshl_or_b32 v23, v168, 14, v167
	v_lshrrev_b32_e32 v168, 1, v164
	v_lshl_or_b32 v23, v168, 13, v23
	v_add_u32_e32 v237, 0x1000, v9
	v_add_u32_e32 v238, 0x2000, v9
	v_add_u32_e32 v239, 0x3000, v9
	v_add_u32_e32 v240, 0x10000, v9
	v_add_u32_e32 v241, 0x11000, v9
	v_add_u32_e32 v242, 0x12000, v9
	v_add_u32_e32 v243, 0x13000, v9
	s_waitcnt lgkmcnt(0)
	s_load_dwordx8 s[40:47], s[8:9], 0x0
	s_load_dwordx2 s[48:49], s[8:9], 0x20
	s_load_dword s50, s[8:9], 0x28
	s_add_u32 s18, s4, s16
	s_addc_u32 s19, s5, 0
	s_add_u32 s20, s6, s16
	s_addc_u32 s21, s7, 0
	global_load_dwordx4 v[36:39], v9, s[18:19] offset:0 sc1 nt
	global_load_dwordx4 v[40:43], v9, s[18:19] offset:2048 sc1 nt
	global_load_dwordx4 v[68:71], v9, s[20:21] offset:0 sc1 nt
	global_load_dwordx4 v[72:75], v9, s[20:21] offset:2048 sc1 nt
	global_load_dwordx4 v[44:47], v237, s[18:19] offset:0 sc1 nt
	global_load_dwordx4 v[48:51], v237, s[18:19] offset:2048 sc1 nt
	global_load_dwordx4 v[76:79], v237, s[20:21] offset:0 sc1 nt
	global_load_dwordx4 v[80:83], v237, s[20:21] offset:2048 sc1 nt
	global_load_dwordx4 v[52:55], v238, s[18:19] offset:0 sc1 nt
	global_load_dwordx4 v[56:59], v238, s[18:19] offset:2048 sc1 nt
	global_load_dwordx4 v[84:87], v238, s[20:21] offset:0 sc1 nt
	global_load_dwordx4 v[88:91], v238, s[20:21] offset:2048 sc1 nt
	global_load_dwordx4 v[60:63], v239, s[18:19] offset:0 sc1 nt
	global_load_dwordx4 v[64:67], v239, s[18:19] offset:2048 sc1 nt
	global_load_dwordx4 v[92:95], v239, s[20:21] offset:0 sc1 nt
	global_load_dwordx4 v[96:99], v239, s[20:21] offset:2048 sc1 nt
	v_mov_b32_e32 v6, s27
	v_mov_b32_e32 v168, 0
	ds_write_b32 v6, v168 offset:0
	ds_write_b32 v6, v168 offset:32
	ds_write_b32 v6, v168 offset:64
	ds_write_b32 v6, v168 offset:96
	v_lshlrev_b32_e32 v167, 3, v164
	v_xor_b32_e32 v168, 16, v167
	v_sub_u32_e32 v165, v167, v169
	v_sub_u32_e32 v166, v168, v169
	v_add_u32_e32 v172, 0, v165
	v_min_u32_e32 v172, 11, v172
	v_lshlrev_b32_e32 v172, 2, v172
	v_add_u32_e32 v173, 1, v165
	v_min_u32_e32 v173, 11, v173
	v_lshlrev_b32_e32 v173, 2, v173
	v_add_u32_e32 v174, 2, v165
	v_min_u32_e32 v174, 11, v174
	v_lshlrev_b32_e32 v174, 2, v174
	v_add_u32_e32 v175, 3, v165
	v_min_u32_e32 v175, 11, v175
	v_lshlrev_b32_e32 v175, 2, v175
	v_add_u32_e32 v176, 4, v165
	v_min_u32_e32 v176, 11, v176
	v_lshlrev_b32_e32 v176, 2, v176
	v_add_u32_e32 v177, 5, v165
	v_min_u32_e32 v177, 11, v177
	v_lshlrev_b32_e32 v177, 2, v177
	v_add_u32_e32 v178, 6, v165
	v_min_u32_e32 v178, 11, v178
	v_lshlrev_b32_e32 v178, 2, v178
	v_add_u32_e32 v179, 7, v165
	v_min_u32_e32 v179, 11, v179
	v_lshlrev_b32_e32 v179, 2, v179
	v_add_u32_e32 v180, 0, v166
	v_min_u32_e32 v180, 11, v180
	v_lshlrev_b32_e32 v180, 2, v180
	v_add_u32_e32 v181, 1, v166
	v_min_u32_e32 v181, 11, v181
	v_lshlrev_b32_e32 v181, 2, v181
	v_add_u32_e32 v182, 2, v166
	v_min_u32_e32 v182, 11, v182
	v_lshlrev_b32_e32 v182, 2, v182
	v_add_u32_e32 v183, 3, v166
	v_min_u32_e32 v183, 11, v183
	v_lshlrev_b32_e32 v183, 2, v183
	v_add_u32_e32 v184, 4, v166
	v_min_u32_e32 v184, 11, v184
	v_lshlrev_b32_e32 v184, 2, v184
	v_add_u32_e32 v185, 5, v166
	v_min_u32_e32 v185, 11, v185
	v_lshlrev_b32_e32 v185, 2, v185
	v_add_u32_e32 v186, 6, v166
	v_min_u32_e32 v186, 11, v186
	v_lshlrev_b32_e32 v186, 2, v186
	v_add_u32_e32 v187, 7, v166
	v_min_u32_e32 v187, 11, v187
	v_lshlrev_b32_e32 v187, 2, v187
	s_cmp_eq_u32 s15, 7
	s_cselect_b32 s22, 0, 0x20000
	s_add_u32 s84, s18, s22
	s_addc_u32 s85, s19, 0
	s_add_u32 s86, s18, s22
	s_addc_u32 s87, s19, 0
	s_add_u32 s86, s86, 0x1000
	s_addc_u32 s87, s87, 0
	s_add_u32 s88, s20, s22
	s_addc_u32 s89, s21, 0
	s_add_u32 s90, s20, s22
	s_addc_u32 s91, s21, 0
	s_add_u32 s90, s90, 0x1000
	s_addc_u32 s91, s91, 0
	s_waitcnt lgkmcnt(0)
	v_writelane_b32 v171, s40, 0
	v_writelane_b32 v171, s41, 1
	v_writelane_b32 v171, s42, 2
	v_writelane_b32 v171, s43, 3
	v_writelane_b32 v171, s44, 4
	v_writelane_b32 v171, s45, 5
	v_writelane_b32 v171, s46, 6
	v_writelane_b32 v171, s47, 7
	v_writelane_b32 v171, s48, 8
	v_writelane_b32 v171, s49, 9
	v_writelane_b32 v171, s50, 10
	v_writelane_b32 v171, 0, 11
	v_fma_mixlo_f16 v171, v171, s51, 0
	ds_bpermute_b32 v188, v172, v171
	ds_bpermute_b32 v189, v173, v171
	ds_bpermute_b32 v190, v174, v171
	ds_bpermute_b32 v191, v175, v171
	ds_bpermute_b32 v192, v176, v171
	ds_bpermute_b32 v193, v177, v171
	ds_bpermute_b32 v194, v178, v171
	ds_bpermute_b32 v195, v179, v171
	v_mov_b32_e32 v229, 0x44800000
	v_fma_mixlo_f16 v228, s40, v229, 0
	v_cvt_f32_f16_e32 v228, v228
	v_cvt_f64_f32_e32 v[212:213], v228
	v_add_f64 v[212:213], v[212:213], 0
	v_fma_mixlo_f16 v228, s41, v229, 0
	v_cvt_f32_f16_e32 v228, v228
	v_cvt_f64_f32_e32 v[214:215], v228
	v_add_f64 v[212:213], v[212:213], v[214:215]
	v_fma_mixlo_f16 v228, s42, v229, 0
	v_cvt_f32_f16_e32 v228, v228
	v_cvt_f64_f32_e32 v[214:215], v228
	v_add_f64 v[212:213], v[212:213], v[214:215]
	v_fma_mixlo_f16 v228, s43, v229, 0
	v_cvt_f32_f16_e32 v228, v228
	v_cvt_f64_f32_e32 v[214:215], v228
	v_add_f64 v[212:213], v[212:213], v[214:215]
	v_fma_mixlo_f16 v228, s44, v229, 0
	v_cvt_f32_f16_e32 v228, v228
	v_cvt_f64_f32_e32 v[214:215], v228
	v_add_f64 v[212:213], v[212:213], v[214:215]
	v_fma_mixlo_f16 v228, s45, v229, 0
	v_cvt_f32_f16_e32 v228, v228
	v_cvt_f64_f32_e32 v[214:215], v228
	v_add_f64 v[212:213], v[212:213], v[214:215]
	v_fma_mixlo_f16 v228, s46, v229, 0
	v_cvt_f32_f16_e32 v228, v228
	v_cvt_f64_f32_e32 v[214:215], v228
	v_add_f64 v[212:213], v[212:213], v[214:215]
	v_fma_mixlo_f16 v228, s47, v229, 0
	v_cvt_f32_f16_e32 v228, v228
	v_cvt_f64_f32_e32 v[214:215], v228
	v_add_f64 v[212:213], v[212:213], v[214:215]
	v_fma_mixlo_f16 v228, s48, v229, 0
	v_cvt_f32_f16_e32 v228, v228
	v_cvt_f64_f32_e32 v[214:215], v228
	v_add_f64 v[212:213], v[212:213], v[214:215]
	v_fma_mixlo_f16 v228, s49, v229, 0
	v_cvt_f32_f16_e32 v228, v228
	v_cvt_f64_f32_e32 v[214:215], v228
	v_add_f64 v[212:213], v[212:213], v[214:215]
	v_fma_mixlo_f16 v228, s50, v229, 0
	v_cvt_f32_f16_e32 v228, v228
	v_cvt_f64_f32_e32 v[214:215], v228
	v_add_f64 v[212:213], v[212:213], v[214:215]
	s_waitcnt lgkmcnt(7)
	ds_bpermute_b32 v196, v180, v171
	ds_bpermute_b32 v197, v181, v171
	ds_bpermute_b32 v198, v182, v171
	ds_bpermute_b32 v199, v183, v171
	ds_bpermute_b32 v200, v184, v171
	ds_bpermute_b32 v201, v185, v171
	ds_bpermute_b32 v202, v186, v171
	ds_bpermute_b32 v203, v187, v171
	v_mul_f64 v[212:213], v[212:213], v[212:213]
	v_mul_f64 v[216:217], v[212:213], 0.5
	v_add_f64 v[218:219], v[216:217], v[216:217]
	s_mov_b32 s36, 0xeb1c432d
	s_mov_b32 s37, 0x3f1a36e2
	v_mul_f64 v[220:221], v[212:213], s[36:37]
	v_mul_f64 v[222:223], v[216:217], v[218:219]
	v_fmac_f64_e32 v[222:223], v[212:213], v[220:221]
	v_add_f64 v[224:225], v[212:213], v[212:213]
	s_mov_b32 s36, 0x487fcb92
	s_mov_b32 s37, 0x3f4d7dbf
	v_mul_f64 v[226:227], v[212:213], s[36:37]
	v_cvt_f32_f64_e32 v0, v[226:227]
	v_mov_b32_e32 v1, v0
	v_mov_b32_e32 v2, v0
	v_mov_b32_e32 v3, v0
	v_cvt_f32_f64_e32 v10, v[218:219]
	v_cvt_f32_f64_e32 v11, v[222:223]
	v_cvt_f32_f64_e32 v12, v[212:213]
	v_cvt_f32_f64_e32 v13, v[224:225]
	v_mul_f64 v[226:227], v[212:213], v[226:227]
	v_cvt_f32_f64_e32 v14, v[226:227]
	v_lshlrev_b32_e32 v167, 2, v164
	s_cmp_eq_u32 s12, 0
	s_cselect_b32 s23, 6, 64
	v_add_u32_e32 v168, 0, v167
	v_cmp_gt_u32_e32 vcc, s23, v168
	s_nop 1
	v_cndmask_b32_e64 v15, 0, 1.0, vcc
	v_add_u32_e32 v168, 1, v167
	v_cmp_gt_u32_e32 vcc, s23, v168
	s_nop 1
	v_cndmask_b32_e64 v16, 0, 1.0, vcc
	v_add_u32_e32 v168, 2, v167
	v_cmp_gt_u32_e32 vcc, s23, v168
	s_nop 1
	v_cndmask_b32_e64 v17, 0, 1.0, vcc
	v_add_u32_e32 v168, 3, v167
	v_cmp_gt_u32_e32 vcc, s23, v168
	s_nop 1
	v_cndmask_b32_e64 v18, 0, 1.0, vcc
	v_and_b32_e32 v167, 31, v8
	v_lshlrev_b32_e32 v167, 4, v167
	s_lshl_b32 s24, s12, 11
	s_add_i32 s25, s12, 7
	s_and_b32 s25, s25, 7
	s_lshl_b32 s26, s25, 11
	v_or_b32_e32 v4, s24, v167
	v_or_b32_e32 v5, s26, v167
	s_lshl_b32 s28, s25, 2
	s_add_u32 s28, s28, 0x10000
	v_mov_b32_e32 v7, s28
	v_mov_b32_e32 v19, 0
	v_mov_b32_e32 v20, 0
	v_mov_b32_e32 v21, 0
	v_mov_b32_e32 v22, 0
	s_waitcnt lgkmcnt(0)
	v_cmp_lt_u32_e64 s[32:33], 31, v8
	v_cmp_gt_u32_e64 s[34:35], 32, v8
	v_pack_b32_f16 v24, v188, v189
	v_pack_b32_f16 v25, v190, v191
	v_pack_b32_f16 v26, v192, v193
	v_pack_b32_f16 v27, v194, v195
	v_pack_b32_f16 v167, v196, v197
	v_cndmask_b32_e64 v28, 0, v167, s[32:33]
	v_cndmask_b32_e64 v32, 0, v167, s[34:35]
	v_pack_b32_f16 v167, v198, v199
	v_cndmask_b32_e64 v29, 0, v167, s[32:33]
	v_cndmask_b32_e64 v33, 0, v167, s[34:35]
	v_pack_b32_f16 v167, v200, v201
	v_cndmask_b32_e64 v30, 0, v167, s[32:33]
	v_cndmask_b32_e64 v34, 0, v167, s[34:35]
	v_pack_b32_f16 v167, v202, v203
	v_cndmask_b32_e64 v31, 0, v167, s[32:33]
	v_cndmask_b32_e64 v35, 0, v167, s[34:35]
	s_waitcnt lgkmcnt(0)
	s_cmp_lt_u32 s12, 4
	s_cbranch_scc1 .Lq_noprio
	s_setprio 1
.Lq_noprio:
	s_waitcnt vmcnt(12)
	v_cvt_pk_f16_f32 v164, v36, v40
	v_cvt_pk_f16_f32 v180, v68, v72
	v_pk_add_f16 v164, v164, -0.5 op_sel_hi:[1,0]
	v_pk_add_f16 v180, v180, -0.5 op_sel_hi:[1,0]
	v_pk_mul_f16 v196, v180, v180
	v_pk_mul_f16 v212, v164, v180
	v_pk_fma_f16 v196, v164, v164, v196
	v_cvt_pk_f16_f32 v168, v37, v41
	v_cvt_pk_f16_f32 v184, v69, v73
	v_pk_add_f16 v168, v168, -0.5 op_sel_hi:[1,0]
	v_pk_add_f16 v184, v184, -0.5 op_sel_hi:[1,0]
	v_pk_mul_f16 v200, v184, v184
	v_pk_mul_f16 v216, v168, v184
	v_pk_fma_f16 v200, v168, v168, v200
	v_cvt_pk_f16_f32 v172, v38, v42
	v_cvt_pk_f16_f32 v188, v70, v74
	v_pk_add_f16 v172, v172, -0.5 op_sel_hi:[1,0]
	v_pk_add_f16 v188, v188, -0.5 op_sel_hi:[1,0]
	v_pk_mul_f16 v204, v188, v188
	v_pk_mul_f16 v220, v172, v188
	v_pk_fma_f16 v204, v172, v172, v204
	v_cvt_pk_f16_f32 v176, v39, v43
	v_cvt_pk_f16_f32 v192, v71, v75
	v_pk_add_f16 v176, v176, -0.5 op_sel_hi:[1,0]
	v_pk_add_f16 v192, v192, -0.5 op_sel_hi:[1,0]
	v_pk_mul_f16 v208, v192, v192
	v_pk_mul_f16 v224, v176, v192
	v_pk_fma_f16 v208, v176, v176, v208
	global_load_dwordx4 v[100:103], v240, s[18:19] offset:0 sc1 nt
	global_load_dwordx4 v[104:107], v240, s[18:19] offset:2048 sc1 nt
	global_load_dwordx4 v[132:135], v240, s[20:21] offset:0 sc1 nt
	global_load_dwordx4 v[136:139], v240, s[20:21] offset:2048 sc1 nt
	global_load_dwordx4 v[108:111], v241, s[18:19] offset:0 sc1 nt
	global_load_dwordx4 v[112:115], v241, s[18:19] offset:2048 sc1 nt
	global_load_dwordx4 v[140:143], v241, s[20:21] offset:0 sc1 nt
	global_load_dwordx4 v[144:147], v241, s[20:21] offset:2048 sc1 nt
	global_load_dwordx4 v[116:119], v242, s[18:19] offset:0 sc1 nt
	global_load_dwordx4 v[120:123], v242, s[18:19] offset:2048 sc1 nt
	global_load_dwordx4 v[148:151], v242, s[20:21] offset:0 sc1 nt
	global_load_dwordx4 v[152:155], v242, s[20:21] offset:2048 sc1 nt
	global_load_dwordx4 v[124:127], v243, s[18:19] offset:0 sc1 nt
	global_load_dwordx4 v[128:131], v243, s[18:19] offset:2048 sc1 nt
	global_load_dwordx4 v[156:159], v243, s[20:21] offset:0 sc1 nt
	global_load_dwordx4 v[160:163], v243, s[20:21] offset:2048 sc1 nt
	s_waitcnt vmcnt(24)
	v_cvt_pk_f16_f32 v165, v44, v48
	v_cvt_pk_f16_f32 v181, v76, v80
	v_pk_add_f16 v165, v165, -0.5 op_sel_hi:[1,0]
	v_pk_add_f16 v181, v181, -0.5 op_sel_hi:[1,0]
	v_pk_mul_f16 v197, v181, v181
	v_pk_mul_f16 v213, v165, v181
	v_pk_fma_f16 v197, v165, v165, v197
	v_cvt_pk_f16_f32 v169, v45, v49
	v_cvt_pk_f16_f32 v185, v77, v81
	v_pk_add_f16 v169, v169, -0.5 op_sel_hi:[1,0]
	v_pk_add_f16 v185, v185, -0.5 op_sel_hi:[1,0]
	v_pk_mul_f16 v201, v185, v185
	v_pk_mul_f16 v217, v169, v185
	v_pk_fma_f16 v201, v169, v169, v201
	v_cvt_pk_f16_f32 v173, v46, v50
	v_cvt_pk_f16_f32 v189, v78, v82
	v_pk_add_f16 v173, v173, -0.5 op_sel_hi:[1,0]
	v_pk_add_f16 v189, v189, -0.5 op_sel_hi:[1,0]
	v_pk_mul_f16 v205, v189, v189
	v_pk_mul_f16 v221, v173, v189
	v_pk_fma_f16 v205, v173, v173, v205
	v_cvt_pk_f16_f32 v177, v47, v51
	v_cvt_pk_f16_f32 v193, v79, v83
	v_pk_add_f16 v177, v177, -0.5 op_sel_hi:[1,0]
	v_pk_add_f16 v193, v193, -0.5 op_sel_hi:[1,0]
	v_pk_mul_f16 v209, v193, v193
	v_pk_mul_f16 v225, v177, v193
	v_pk_fma_f16 v209, v177, v177, v209
	s_waitcnt vmcnt(20)
	v_cvt_pk_f16_f32 v166, v52, v56
	v_cvt_pk_f16_f32 v182, v84, v88
	v_pk_add_f16 v166, v166, -0.5 op_sel_hi:[1,0]
	v_pk_add_f16 v182, v182, -0.5 op_sel_hi:[1,0]
	v_pk_mul_f16 v198, v182, v182
	v_pk_mul_f16 v214, v166, v182
	v_pk_fma_f16 v198, v166, v166, v198
	v_cvt_pk_f16_f32 v170, v53, v57
	v_cvt_pk_f16_f32 v186, v85, v89
	v_pk_add_f16 v170, v170, -0.5 op_sel_hi:[1,0]
	v_pk_add_f16 v186, v186, -0.5 op_sel_hi:[1,0]
	v_pk_mul_f16 v202, v186, v186
	v_pk_mul_f16 v218, v170, v186
	v_pk_fma_f16 v202, v170, v170, v202
	v_cvt_pk_f16_f32 v174, v54, v58
	v_cvt_pk_f16_f32 v190, v86, v90
	v_pk_add_f16 v174, v174, -0.5 op_sel_hi:[1,0]
	v_pk_add_f16 v190, v190, -0.5 op_sel_hi:[1,0]
	v_pk_mul_f16 v206, v190, v190
	v_pk_mul_f16 v222, v174, v190
	v_pk_fma_f16 v206, v174, v174, v206
	v_cvt_pk_f16_f32 v178, v55, v59
	v_cvt_pk_f16_f32 v194, v87, v91
	v_pk_add_f16 v178, v178, -0.5 op_sel_hi:[1,0]
	v_pk_add_f16 v194, v194, -0.5 op_sel_hi:[1,0]
	v_pk_mul_f16 v210, v194, v194
	v_pk_mul_f16 v226, v178, v194
	v_pk_fma_f16 v210, v178, v178, v210
	s_waitcnt vmcnt(16)
	v_cvt_pk_f16_f32 v167, v60, v64
	v_cvt_pk_f16_f32 v183, v92, v96
	v_pk_add_f16 v167, v167, -0.5 op_sel_hi:[1,0]
	v_pk_add_f16 v183, v183, -0.5 op_sel_hi:[1,0]
	v_pk_mul_f16 v199, v183, v183
	v_pk_mul_f16 v215, v167, v183
	v_pk_fma_f16 v199, v167, v167, v199
	v_cvt_pk_f16_f32 v171, v61, v65
	v_cvt_pk_f16_f32 v187, v93, v97
	v_pk_add_f16 v171, v171, -0.5 op_sel_hi:[1,0]
	v_pk_add_f16 v187, v187, -0.5 op_sel_hi:[1,0]
	v_pk_mul_f16 v203, v187, v187
	v_pk_mul_f16 v219, v171, v187
	v_pk_fma_f16 v203, v171, v171, v203
	v_cvt_pk_f16_f32 v175, v62, v66
	v_cvt_pk_f16_f32 v191, v94, v98
	v_pk_add_f16 v175, v175, -0.5 op_sel_hi:[1,0]
	v_pk_add_f16 v191, v191, -0.5 op_sel_hi:[1,0]
	v_pk_mul_f16 v207, v191, v191
	v_pk_mul_f16 v223, v175, v191
	v_pk_fma_f16 v207, v175, v175, v207
	v_cvt_pk_f16_f32 v179, v63, v67
	v_cvt_pk_f16_f32 v195, v95, v99
	v_pk_add_f16 v179, v179, -0.5 op_sel_hi:[1,0]
	v_pk_add_f16 v195, v195, -0.5 op_sel_hi:[1,0]
	v_pk_mul_f16 v211, v195, v195
	v_pk_mul_f16 v227, v179, v195
	v_pk_fma_f16 v211, v179, v179, v211
	v_mfma_f32_16x16x32_f16 v[68:71], v[164:167], v[24:27], 0
	v_mfma_f32_16x16x32_f16 v[72:75], v[168:171], v[24:27], 0
	v_mfma_f32_16x16x32_f16 v[76:79], v[172:175], v[24:27], 0
	v_mfma_f32_16x16x32_f16 v[80:83], v[176:179], v[24:27], 0
	v_mfma_f32_16x16x32_f16 v[84:87], v[180:183], v[24:27], 0
	v_mfma_f32_16x16x32_f16 v[88:91], v[184:187], v[24:27], 0
	v_mfma_f32_16x16x32_f16 v[92:95], v[188:191], v[24:27], 0
	v_mfma_f32_16x16x32_f16 v[96:99], v[192:195], v[24:27], 0
	s_nop 1
	v_cvt_pk_f16_f32 v36, v68, v72
	s_nop 0
	v_cvt_pk_f16_f32 v37, v76, v80
	v_cvt_pk_f16_f32 v38, v69, v73
	v_cvt_pk_f16_f32 v39, v77, v81
	v_cvt_pk_f16_f32 v40, v70, v74
	v_cvt_pk_f16_f32 v41, v78, v82
	v_cvt_pk_f16_f32 v42, v71, v75
	v_cvt_pk_f16_f32 v43, v79, v83
	v_mfma_f32_16x16x32_f16 v[68:71], v[196:199], v[24:27], 0
	v_mfma_f32_16x16x32_f16 v[72:75], v[200:203], v[24:27], 0
	v_mfma_f32_16x16x32_f16 v[76:79], v[204:207], v[24:27], 0
	v_mfma_f32_16x16x32_f16 v[80:83], v[208:211], v[24:27], 0
	v_cvt_pk_f16_f32 v44, v84, v88
	v_cvt_pk_f16_f32 v45, v92, v96
	v_cvt_pk_f16_f32 v46, v85, v89
	v_cvt_pk_f16_f32 v47, v93, v97
	v_cvt_pk_f16_f32 v48, v86, v90
	v_cvt_pk_f16_f32 v49, v94, v98
	v_cvt_pk_f16_f32 v50, v87, v91
	v_cvt_pk_f16_f32 v51, v95, v99
	v_mfma_f32_16x16x32_f16 v[84:87], v[212:215], v[24:27], 0
	v_mfma_f32_16x16x32_f16 v[88:91], v[216:219], v[24:27], 0
	v_mfma_f32_16x16x32_f16 v[92:95], v[220:223], v[24:27], 0
	v_mfma_f32_16x16x32_f16 v[96:99], v[224:227], v[24:27], 0
	v_cvt_pk_f16_f32 v52, v68, v72
	v_cvt_pk_f16_f32 v53, v76, v80
	v_cvt_pk_f16_f32 v54, v69, v73
	v_cvt_pk_f16_f32 v55, v77, v81
	v_cvt_pk_f16_f32 v56, v70, v74
	v_cvt_pk_f16_f32 v57, v78, v82
	v_cvt_pk_f16_f32 v58, v71, v75
	v_cvt_pk_f16_f32 v59, v79, v83
	v_cvt_pk_f16_f32 v60, v84, v88
	v_cvt_pk_f16_f32 v61, v92, v96
	v_cvt_pk_f16_f32 v62, v85, v89
	v_cvt_pk_f16_f32 v63, v93, v97
	v_cvt_pk_f16_f32 v64, v86, v90
	v_cvt_pk_f16_f32 v65, v94, v98
	v_cvt_pk_f16_f32 v66, v87, v91
	v_cvt_pk_f16_f32 v67, v95, v99
	s_mov_b64 exec, s[38:39]
	ds_write_b128 v4, v[40:43] offset:0
	ds_write_b128 v4, v[48:51] offset:512
	ds_write_b128 v4, v[56:59] offset:1024
	ds_write_b128 v4, v[64:67] offset:1536
	s_mov_b64 exec, -1
	v_mfma_f32_16x16x32_f16 v[68:71], v[24:27], v[36:39], 0
	v_mfma_f32_16x16x32_f16 v[72:75], v[24:27], v[44:47], 0
	v_mfma_f32_16x16x32_f16 v[76:79], v[24:27], v[52:55], v[0:3]
	v_mfma_f32_16x16x32_f16 v[80:83], v[24:27], v[60:63], 0
	v_mfma_f32_16x16x32_f16 v[84:87], v[28:31], v[36:39], 0
	v_mfma_f32_16x16x32_f16 v[88:91], v[28:31], v[44:47], 0
	v_mfma_f32_16x16x32_f16 v[92:95], v[28:31], v[52:55], v[0:3]
	v_mfma_f32_16x16x32_f16 v[96:99], v[28:31], v[60:63], 0
	v_mfma_f32_16x16x32_f16 v[84:87], v[32:35], v[40:43], v[84:87]
	v_mfma_f32_16x16x32_f16 v[88:91], v[32:35], v[48:51], v[88:91]
	v_mfma_f32_16x16x32_f16 v[92:95], v[32:35], v[56:59], v[92:95]
	v_mfma_f32_16x16x32_f16 v[96:99], v[32:35], v[64:67], v[96:99]
	s_waitcnt lgkmcnt(0)
	ds_write_b32 v6, v6 offset:0
	ds_read_b32 v9, v7 offset:0
	v_mul_f32_e32 v244, v68, v72
	v_mul_f32_e32 v250, v69, v73
	v_mul_f32_e64 v245, -v72, v72
	v_mul_f32_e64 v251, -v73, v73
	v_add_f32_e32 v246, v68, v72
	v_add_f32_e32 v252, v69, v73
	v_fma_f32 v245, -v68, v68, v245
	v_fma_f32 v251, -v69, v69, v251
	v_fma_f32 v247, v10, v246, v11
	v_fma_f32 v253, v10, v252, v11
	v_fma_f32 v246, v13, v80, v14
	v_fma_f32 v252, v13, v81, v14
	v_fma_f32 v248, v12, v76, v245
	v_fma_f32 v254, v12, v77, v251
	v_fma_f32 v249, 2.0, v244, v247
	v_fma_f32 v255, 2.0, v250, v253
	v_sub_f32_e32 v247, v247, v245
	v_sub_f32_e32 v253, v253, v251
	v_fma_f32 v246, -2.0, v244, v246
	v_fma_f32 v252, -2.0, v250, v252
	v_mul_f32_e32 v247, v247, v248
	v_mul_f32_e32 v253, v253, v254
	v_rcp_f32_e32 v247, v247
	v_rcp_f32_e32 v253, v253
	v_mul_f32_e32 v249, v249, v246
	v_mul_f32_e32 v255, v255, v252
	v_fma_f32 v19, v249, v247, v19
	v_fma_f32 v19, v255, v253, v19
	v_mul_f32_e32 v244, v70, v74
	v_mul_f32_e32 v250, v71, v75
	v_mul_f32_e64 v245, -v74, v74
	v_mul_f32_e64 v251, -v75, v75
	v_add_f32_e32 v246, v70, v74
	v_add_f32_e32 v252, v71, v75
	v_fma_f32 v245, -v70, v70, v245
	v_fma_f32 v251, -v71, v71, v251
	v_fma_f32 v247, v10, v246, v11
	v_fma_f32 v253, v10, v252, v11
	v_fma_f32 v246, v13, v82, v14
	v_fma_f32 v252, v13, v83, v14
	v_fma_f32 v248, v12, v78, v245
	v_fma_f32 v254, v12, v79, v251
	v_fma_f32 v249, 2.0, v244, v247
	v_fma_f32 v255, 2.0, v250, v253
	v_sub_f32_e32 v247, v247, v245
	v_sub_f32_e32 v253, v253, v251
	v_fma_f32 v246, -2.0, v244, v246
	v_fma_f32 v252, -2.0, v250, v252
	v_mul_f32_e32 v247, v247, v248
	v_mul_f32_e32 v253, v253, v254
	v_rcp_f32_e32 v247, v247
	v_rcp_f32_e32 v253, v253
	v_mul_f32_e32 v249, v249, v246
	v_mul_f32_e32 v255, v255, v252
	v_fma_f32 v20, v249, v247, v20
	v_fma_f32 v20, v255, v253, v20
	v_mfma_f32_16x16x32_f16 v[68:71], v[24:27], v[40:43], 0
	v_mfma_f32_16x16x32_f16 v[72:75], v[24:27], v[48:51], 0
	v_mfma_f32_16x16x32_f16 v[76:79], v[24:27], v[56:59], v[0:3]
	v_mfma_f32_16x16x32_f16 v[80:83], v[24:27], v[64:67], 0
	s_barrier
	ds_read_b32 v9, v7 offset:0
	s_waitcnt lgkmcnt(0)
	v_cmp_ne_u32_e32 vcc, 0, v9
	s_cbranch_vccnz .Lq_go_0
